# speedup vs baseline: 1.0086x; 1.0030x over previous
.Lex_skip:
.LBB5_148:
	s_or_b32 s2, s49, s28
	s_lshl_b32 s0, s2, 12
	s_mov_b32 s1, 0
	v_lshl_add_u64 v[176:177], v[166:167], 0, s[0:1]
	s_waitcnt vmcnt(0)
	s_waitcnt vmcnt(0) lgkmcnt(0)
	s_barrier
	global_load_dwordx4 v[162:165], v[176:177], off
	global_load_dwordx4 v[168:171], v[176:177], off offset:1024
	global_load_dwordx4 v[172:175], v[176:177], off offset:2048
	s_nop 0
	global_load_dwordx4 v[176:179], v[176:177], off offset:3072
	v_lshl_add_u32 v208, s51, 10, v191
	ds_read_b128 v[192:195], v208
	ds_read_b128 v[196:199], v208 offset:16384
	ds_read_b128 v[200:203], v208 offset:32768
	ds_read_b128 v[204:207], v208 offset:49152
	s_setprio 1
	s_waitcnt lgkmcnt(3)
	v_mfma_f32_16x16x32_f16 v[34:37], v[2:5], v[192:195], v[34:37]
	v_mfma_f32_16x16x32_f16 v[38:41], v[6:9], v[192:195], v[38:41]
	v_mfma_f32_16x16x32_f16 v[42:45], v[10:13], v[192:195], v[42:45]
	v_mfma_f32_16x16x32_f16 v[46:49], v[14:17], v[192:195], v[46:49]
	s_waitcnt lgkmcnt(2)
	v_mfma_f32_16x16x32_f16 v[50:53], v[2:5], v[196:199], v[50:53]
	v_mfma_f32_16x16x32_f16 v[54:57], v[6:9], v[196:199], v[54:57]
	v_mfma_f32_16x16x32_f16 v[58:61], v[10:13], v[196:199], v[58:61]
	v_mfma_f32_16x16x32_f16 v[62:65], v[14:17], v[196:199], v[62:65]
	s_waitcnt lgkmcnt(1)
	v_mfma_f32_16x16x32_f16 v[66:69], v[2:5], v[200:203], v[66:69]
	v_mfma_f32_16x16x32_f16 v[70:73], v[6:9], v[200:203], v[70:73]
	v_mfma_f32_16x16x32_f16 v[74:77], v[10:13], v[200:203], v[74:77]
	v_mfma_f32_16x16x32_f16 v[78:81], v[14:17], v[200:203], v[78:81]
	s_waitcnt lgkmcnt(0)
	v_mfma_f32_16x16x32_f16 v[82:85], v[2:5], v[204:207], v[82:85]
	v_mfma_f32_16x16x32_f16 v[86:89], v[6:9], v[204:207], v[86:89]
	v_mfma_f32_16x16x32_f16 v[90:93], v[10:13], v[204:207], v[90:93]
	v_mfma_f32_16x16x32_f16 v[94:97], v[14:17], v[204:207], v[94:97]
	s_setprio 0
	v_add_u32_e32 v192, 0x10000, v208
	v_add_u32_e32 v196, 0x14000, v208
	v_add_u32_e32 v200, 0x18000, v208
	v_add_u32_e32 v204, 0x1c000, v208
	ds_read_b128 v[192:195], v192
	ds_read_b128 v[196:199], v196
	ds_read_b128 v[200:203], v200
	ds_read_b128 v[204:207], v204
	s_setprio 1
	s_waitcnt lgkmcnt(3)
	v_mfma_f32_16x16x32_f16 v[98:101], v[2:5], v[192:195], v[98:101]
	v_mfma_f32_16x16x32_f16 v[102:105], v[6:9], v[192:195], v[102:105]
	v_mfma_f32_16x16x32_f16 v[106:109], v[10:13], v[192:195], v[106:109]
	v_mfma_f32_16x16x32_f16 v[110:113], v[14:17], v[192:195], v[110:113]
	s_waitcnt lgkmcnt(2)
	v_mfma_f32_16x16x32_f16 v[114:117], v[2:5], v[196:199], v[114:117]
	v_mfma_f32_16x16x32_f16 v[118:121], v[6:9], v[196:199], v[118:121]
	v_mfma_f32_16x16x32_f16 v[122:125], v[10:13], v[196:199], v[122:125]
	v_mfma_f32_16x16x32_f16 v[126:129], v[14:17], v[196:199], v[126:129]
	s_waitcnt lgkmcnt(1)
	v_mfma_f32_16x16x32_f16 v[130:133], v[2:5], v[200:203], v[130:133]
	v_mfma_f32_16x16x32_f16 v[134:137], v[6:9], v[200:203], v[134:137]
	v_mfma_f32_16x16x32_f16 v[138:141], v[10:13], v[200:203], v[138:141]
	v_mfma_f32_16x16x32_f16 v[142:145], v[14:17], v[200:203], v[142:145]
	s_waitcnt lgkmcnt(0)
	v_mfma_f32_16x16x32_f16 v[2:5], v[2:5], v[204:207], v[146:149]
	v_mfma_f32_16x16x32_f16 v[6:9], v[6:9], v[204:207], v[150:153]
	v_mfma_f32_16x16x32_f16 v[10:13], v[10:13], v[204:207], v[154:157]
	v_mfma_f32_16x16x32_f16 v[14:17], v[14:17], v[204:207], v[158:161]
	s_setprio 0
	s_or_b32 s3, s49, s29
	s_lshl_b32 s0, s3, 12
	v_lshl_add_u64 v[158:159], v[166:167], 0, s[0:1]
	global_load_dwordx4 v[146:149], v[158:159], off
	global_load_dwordx4 v[150:153], v[158:159], off offset:1024
	global_load_dwordx4 v[154:157], v[158:159], off offset:2048
	s_nop 0
	global_load_dwordx4 v[158:161], v[158:159], off offset:3072
	v_lshl_add_u32 v208, s52, 10, v191
	ds_read_b128 v[192:195], v208
	ds_read_b128 v[196:199], v208 offset:16384
	ds_read_b128 v[200:203], v208 offset:32768
	ds_read_b128 v[204:207], v208 offset:49152
	s_setprio 1
	s_waitcnt lgkmcnt(3)
	v_mfma_f32_16x16x32_f16 v[34:37], v[18:21], v[192:195], v[34:37]
	v_mfma_f32_16x16x32_f16 v[38:41], v[22:25], v[192:195], v[38:41]
	v_mfma_f32_16x16x32_f16 v[42:45], v[26:29], v[192:195], v[42:45]
	v_mfma_f32_16x16x32_f16 v[46:49], v[30:33], v[192:195], v[46:49]
	s_waitcnt lgkmcnt(2)
	v_mfma_f32_16x16x32_f16 v[50:53], v[18:21], v[196:199], v[50:53]
	v_mfma_f32_16x16x32_f16 v[54:57], v[22:25], v[196:199], v[54:57]
	v_mfma_f32_16x16x32_f16 v[58:61], v[26:29], v[196:199], v[58:61]
	v_mfma_f32_16x16x32_f16 v[62:65], v[30:33], v[196:199], v[62:65]
	s_waitcnt lgkmcnt(1)
	v_mfma_f32_16x16x32_f16 v[66:69], v[18:21], v[200:203], v[66:69]
	v_mfma_f32_16x16x32_f16 v[70:73], v[22:25], v[200:203], v[70:73]
	v_mfma_f32_16x16x32_f16 v[74:77], v[26:29], v[200:203], v[74:77]
	v_mfma_f32_16x16x32_f16 v[78:81], v[30:33], v[200:203], v[78:81]
	s_waitcnt lgkmcnt(0)
	v_mfma_f32_16x16x32_f16 v[82:85], v[18:21], v[204:207], v[82:85]
	v_mfma_f32_16x16x32_f16 v[86:89], v[22:25], v[204:207], v[86:89]
	v_mfma_f32_16x16x32_f16 v[90:93], v[26:29], v[204:207], v[90:93]
	v_mfma_f32_16x16x32_f16 v[94:97], v[30:33], v[204:207], v[94:97]
	s_setprio 0
	v_add_u32_e32 v192, 0x10000, v208
	v_add_u32_e32 v196, 0x14000, v208
	v_add_u32_e32 v200, 0x18000, v208
	v_add_u32_e32 v204, 0x1c000, v208
	ds_read_b128 v[192:195], v192
	ds_read_b128 v[196:199], v196
	ds_read_b128 v[200:203], v200
	ds_read_b128 v[204:207], v204
	s_setprio 1
	s_waitcnt lgkmcnt(3)
	v_mfma_f32_16x16x32_f16 v[98:101], v[18:21], v[192:195], v[98:101]
	v_mfma_f32_16x16x32_f16 v[102:105], v[22:25], v[192:195], v[102:105]
	v_mfma_f32_16x16x32_f16 v[106:109], v[26:29], v[192:195], v[106:109]
	v_mfma_f32_16x16x32_f16 v[110:113], v[30:33], v[192:195], v[110:113]
	s_waitcnt lgkmcnt(2)
	v_mfma_f32_16x16x32_f16 v[114:117], v[18:21], v[196:199], v[114:117]
	v_mfma_f32_16x16x32_f16 v[118:121], v[22:25], v[196:199], v[118:121]
	v_mfma_f32_16x16x32_f16 v[122:125], v[26:29], v[196:199], v[122:125]
	v_mfma_f32_16x16x32_f16 v[126:129], v[30:33], v[196:199], v[126:129]
	s_waitcnt lgkmcnt(1)
	v_mfma_f32_16x16x32_f16 v[130:133], v[18:21], v[200:203], v[130:133]
	v_mfma_f32_16x16x32_f16 v[134:137], v[22:25], v[200:203], v[134:137]
	v_mfma_f32_16x16x32_f16 v[138:141], v[26:29], v[200:203], v[138:141]
	s_waitcnt lgkmcnt(0)
	v_mfma_f32_16x16x32_f16 v[2:5], v[18:21], v[204:207], v[2:5]
	v_mfma_f32_16x16x32_f16 v[6:9], v[22:25], v[204:207], v[6:9]
	v_mfma_f32_16x16x32_f16 v[10:13], v[26:29], v[204:207], v[10:13]
	v_mfma_f32_16x16x32_f16 v[14:17], v[30:33], v[204:207], v[14:17]
	v_mfma_f32_16x16x32_f16 v[142:145], v[30:33], v[200:203], v[142:145]
	s_setprio 0
	s_xor_b32 s7, s51, 4
	s_lshl_b32 s0, s7, 12
	v_lshl_add_u64 v[30:31], v[166:167], 0, s[0:1]
	global_load_dwordx4 v[18:21], v[30:31], off
	global_load_dwordx4 v[22:25], v[30:31], off offset:1024
	global_load_dwordx4 v[26:29], v[30:31], off offset:2048
	s_nop 0
	global_load_dwordx4 v[30:33], v[30:31], off offset:3072
	v_lshl_add_u32 v208, s2, 10, v191
	ds_read_b128 v[192:195], v208
	ds_read_b128 v[196:199], v208 offset:16384
	ds_read_b128 v[200:203], v208 offset:32768
	ds_read_b128 v[204:207], v208 offset:49152
	s_setprio 1
	s_waitcnt vmcnt(11) lgkmcnt(3)
	v_mfma_f32_16x16x32_f16 v[34:37], v[162:165], v[192:195], v[34:37]
	s_waitcnt vmcnt(10)
	v_mfma_f32_16x16x32_f16 v[38:41], v[168:171], v[192:195], v[38:41]
	s_waitcnt vmcnt(9)
	v_mfma_f32_16x16x32_f16 v[42:45], v[172:175], v[192:195], v[42:45]
	s_waitcnt vmcnt(8)
	v_mfma_f32_16x16x32_f16 v[46:49], v[176:179], v[192:195], v[46:49]
	s_waitcnt lgkmcnt(2)
	v_mfma_f32_16x16x32_f16 v[50:53], v[162:165], v[196:199], v[50:53]
	v_mfma_f32_16x16x32_f16 v[54:57], v[168:171], v[196:199], v[54:57]
	v_mfma_f32_16x16x32_f16 v[58:61], v[172:175], v[196:199], v[58:61]
	v_mfma_f32_16x16x32_f16 v[62:65], v[176:179], v[196:199], v[62:65]
	s_waitcnt lgkmcnt(1)
	v_mfma_f32_16x16x32_f16 v[66:69], v[162:165], v[200:203], v[66:69]
	v_mfma_f32_16x16x32_f16 v[70:73], v[168:171], v[200:203], v[70:73]
	v_mfma_f32_16x16x32_f16 v[74:77], v[172:175], v[200:203], v[74:77]
	v_mfma_f32_16x16x32_f16 v[78:81], v[176:179], v[200:203], v[78:81]
	s_waitcnt lgkmcnt(0)
	v_mfma_f32_16x16x32_f16 v[82:85], v[162:165], v[204:207], v[82:85]
	v_mfma_f32_16x16x32_f16 v[86:89], v[168:171], v[204:207], v[86:89]
	v_mfma_f32_16x16x32_f16 v[90:93], v[172:175], v[204:207], v[90:93]
	v_mfma_f32_16x16x32_f16 v[94:97], v[176:179], v[204:207], v[94:97]
	s_setprio 0
	v_add_u32_e32 v192, 0x10000, v208
	v_add_u32_e32 v196, 0x14000, v208
	v_add_u32_e32 v200, 0x18000, v208
	v_add_u32_e32 v204, 0x1c000, v208
	ds_read_b128 v[192:195], v192
	ds_read_b128 v[196:199], v196
	ds_read_b128 v[200:203], v200
	ds_read_b128 v[204:207], v204
	s_setprio 1
	s_waitcnt lgkmcnt(3)
	v_mfma_f32_16x16x32_f16 v[98:101], v[162:165], v[192:195], v[98:101]
	v_mfma_f32_16x16x32_f16 v[102:105], v[168:171], v[192:195], v[102:105]
	v_mfma_f32_16x16x32_f16 v[106:109], v[172:175], v[192:195], v[106:109]
	v_mfma_f32_16x16x32_f16 v[110:113], v[176:179], v[192:195], v[110:113]
	s_waitcnt lgkmcnt(2)
	v_mfma_f32_16x16x32_f16 v[114:117], v[162:165], v[196:199], v[114:117]
	v_mfma_f32_16x16x32_f16 v[118:121], v[168:171], v[196:199], v[118:121]
	v_mfma_f32_16x16x32_f16 v[122:125], v[172:175], v[196:199], v[122:125]
	v_mfma_f32_16x16x32_f16 v[126:129], v[176:179], v[196:199], v[126:129]
	s_waitcnt lgkmcnt(1)
	v_mfma_f32_16x16x32_f16 v[130:133], v[162:165], v[200:203], v[130:133]
	v_mfma_f32_16x16x32_f16 v[134:137], v[168:171], v[200:203], v[134:137]
	v_mfma_f32_16x16x32_f16 v[138:141], v[172:175], v[200:203], v[138:141]
	s_waitcnt lgkmcnt(0)
	v_mfma_f32_16x16x32_f16 v[2:5], v[162:165], v[204:207], v[2:5]
	v_mfma_f32_16x16x32_f16 v[6:9], v[168:171], v[204:207], v[6:9]
	v_mfma_f32_16x16x32_f16 v[10:13], v[172:175], v[204:207], v[10:13]
	v_mfma_f32_16x16x32_f16 v[14:17], v[176:179], v[204:207], v[14:17]
	v_mfma_f32_16x16x32_f16 v[142:145], v[176:179], v[200:203], v[142:145]
	s_setprio 0
	s_or_b32 s2, s49, s30
	s_lshl_b32 s0, s2, 12
	v_lshl_add_u64 v[176:177], v[166:167], 0, s[0:1]
	global_load_dwordx4 v[162:165], v[176:177], off
	global_load_dwordx4 v[168:171], v[176:177], off offset:1024
	global_load_dwordx4 v[172:175], v[176:177], off offset:2048
	s_nop 0
	global_load_dwordx4 v[176:179], v[176:177], off offset:3072
	v_lshl_add_u32 v208, s3, 10, v191
	ds_read_b128 v[192:195], v208
	ds_read_b128 v[196:199], v208 offset:16384
	ds_read_b128 v[200:203], v208 offset:32768
	ds_read_b128 v[204:207], v208 offset:49152
	s_setprio 1
	s_waitcnt vmcnt(11) lgkmcnt(3)
	v_mfma_f32_16x16x32_f16 v[34:37], v[146:149], v[192:195], v[34:37]
	s_waitcnt vmcnt(10)
	v_mfma_f32_16x16x32_f16 v[38:41], v[150:153], v[192:195], v[38:41]
	s_waitcnt vmcnt(9)
	v_mfma_f32_16x16x32_f16 v[42:45], v[154:157], v[192:195], v[42:45]
	s_waitcnt vmcnt(8)
	v_mfma_f32_16x16x32_f16 v[46:49], v[158:161], v[192:195], v[46:49]
	s_waitcnt lgkmcnt(2)
	v_mfma_f32_16x16x32_f16 v[50:53], v[146:149], v[196:199], v[50:53]
	v_mfma_f32_16x16x32_f16 v[54:57], v[150:153], v[196:199], v[54:57]
	v_mfma_f32_16x16x32_f16 v[58:61], v[154:157], v[196:199], v[58:61]
	v_mfma_f32_16x16x32_f16 v[62:65], v[158:161], v[196:199], v[62:65]
	s_waitcnt lgkmcnt(1)
	v_mfma_f32_16x16x32_f16 v[66:69], v[146:149], v[200:203], v[66:69]
	v_mfma_f32_16x16x32_f16 v[70:73], v[150:153], v[200:203], v[70:73]
	v_mfma_f32_16x16x32_f16 v[74:77], v[154:157], v[200:203], v[74:77]
	v_mfma_f32_16x16x32_f16 v[78:81], v[158:161], v[200:203], v[78:81]
	s_waitcnt lgkmcnt(0)
	v_mfma_f32_16x16x32_f16 v[82:85], v[146:149], v[204:207], v[82:85]
	v_mfma_f32_16x16x32_f16 v[86:89], v[150:153], v[204:207], v[86:89]
	v_mfma_f32_16x16x32_f16 v[90:93], v[154:157], v[204:207], v[90:93]
	v_mfma_f32_16x16x32_f16 v[94:97], v[158:161], v[204:207], v[94:97]
	s_setprio 0
	v_add_u32_e32 v192, 0x10000, v208
	v_add_u32_e32 v196, 0x14000, v208
	v_add_u32_e32 v200, 0x18000, v208
	v_add_u32_e32 v204, 0x1c000, v208
	ds_read_b128 v[192:195], v192
	ds_read_b128 v[196:199], v196
	ds_read_b128 v[200:203], v200
	ds_read_b128 v[204:207], v204
	s_setprio 1
	s_waitcnt lgkmcnt(3)
	v_mfma_f32_16x16x32_f16 v[98:101], v[146:149], v[192:195], v[98:101]
	v_mfma_f32_16x16x32_f16 v[102:105], v[150:153], v[192:195], v[102:105]
	v_mfma_f32_16x16x32_f16 v[106:109], v[154:157], v[192:195], v[106:109]
	v_mfma_f32_16x16x32_f16 v[110:113], v[158:161], v[192:195], v[110:113]
	s_waitcnt lgkmcnt(2)
	v_mfma_f32_16x16x32_f16 v[114:117], v[146:149], v[196:199], v[114:117]
	v_mfma_f32_16x16x32_f16 v[118:121], v[150:153], v[196:199], v[118:121]
	v_mfma_f32_16x16x32_f16 v[122:125], v[154:157], v[196:199], v[122:125]
	v_mfma_f32_16x16x32_f16 v[126:129], v[158:161], v[196:199], v[126:129]
	s_waitcnt lgkmcnt(1)
	v_mfma_f32_16x16x32_f16 v[130:133], v[146:149], v[200:203], v[130:133]
	v_mfma_f32_16x16x32_f16 v[134:137], v[150:153], v[200:203], v[134:137]
	v_mfma_f32_16x16x32_f16 v[138:141], v[154:157], v[200:203], v[138:141]
	s_waitcnt lgkmcnt(0)
	v_mfma_f32_16x16x32_f16 v[2:5], v[146:149], v[204:207], v[2:5]
	v_mfma_f32_16x16x32_f16 v[6:9], v[150:153], v[204:207], v[6:9]
	v_mfma_f32_16x16x32_f16 v[10:13], v[154:157], v[204:207], v[10:13]
	v_mfma_f32_16x16x32_f16 v[14:17], v[158:161], v[204:207], v[14:17]
	v_mfma_f32_16x16x32_f16 v[142:145], v[158:161], v[200:203], v[142:145]
	s_setprio 0
	s_or_b32 s3, s49, s31
	s_lshl_b32 s0, s3, 12
	v_lshl_add_u64 v[158:159], v[166:167], 0, s[0:1]
	global_load_dwordx4 v[146:149], v[158:159], off
	global_load_dwordx4 v[150:153], v[158:159], off offset:1024
	global_load_dwordx4 v[154:157], v[158:159], off offset:2048
	s_nop 0
	global_load_dwordx4 v[158:161], v[158:159], off offset:3072
	v_lshl_add_u32 v208, s7, 10, v191
	ds_read_b128 v[192:195], v208
	ds_read_b128 v[196:199], v208 offset:16384
	ds_read_b128 v[200:203], v208 offset:32768
	ds_read_b128 v[204:207], v208 offset:49152
	s_setprio 1
	s_waitcnt vmcnt(11) lgkmcnt(3)
	v_mfma_f32_16x16x32_f16 v[34:37], v[18:21], v[192:195], v[34:37]
	s_waitcnt vmcnt(10)
	v_mfma_f32_16x16x32_f16 v[38:41], v[22:25], v[192:195], v[38:41]
	s_waitcnt vmcnt(9)
	v_mfma_f32_16x16x32_f16 v[42:45], v[26:29], v[192:195], v[42:45]
	s_waitcnt vmcnt(8)
	v_mfma_f32_16x16x32_f16 v[46:49], v[30:33], v[192:195], v[46:49]
	s_waitcnt lgkmcnt(2)
	v_mfma_f32_16x16x32_f16 v[50:53], v[18:21], v[196:199], v[50:53]
	v_mfma_f32_16x16x32_f16 v[54:57], v[22:25], v[196:199], v[54:57]
	v_mfma_f32_16x16x32_f16 v[58:61], v[26:29], v[196:199], v[58:61]
	v_mfma_f32_16x16x32_f16 v[62:65], v[30:33], v[196:199], v[62:65]
	s_waitcnt lgkmcnt(1)
	v_mfma_f32_16x16x32_f16 v[66:69], v[18:21], v[200:203], v[66:69]
	v_mfma_f32_16x16x32_f16 v[70:73], v[22:25], v[200:203], v[70:73]
	v_mfma_f32_16x16x32_f16 v[74:77], v[26:29], v[200:203], v[74:77]
	v_mfma_f32_16x16x32_f16 v[78:81], v[30:33], v[200:203], v[78:81]
	s_waitcnt lgkmcnt(0)
	v_mfma_f32_16x16x32_f16 v[82:85], v[18:21], v[204:207], v[82:85]
	v_mfma_f32_16x16x32_f16 v[86:89], v[22:25], v[204:207], v[86:89]
	v_mfma_f32_16x16x32_f16 v[90:93], v[26:29], v[204:207], v[90:93]
	v_mfma_f32_16x16x32_f16 v[94:97], v[30:33], v[204:207], v[94:97]
	s_setprio 0
	v_add_u32_e32 v192, 0x10000, v208
	v_add_u32_e32 v196, 0x14000, v208
	v_add_u32_e32 v200, 0x18000, v208
	v_add_u32_e32 v204, 0x1c000, v208
	ds_read_b128 v[192:195], v192
	ds_read_b128 v[196:199], v196
	ds_read_b128 v[200:203], v200
	ds_read_b128 v[204:207], v204
	s_setprio 1
	s_waitcnt lgkmcnt(3)
	v_mfma_f32_16x16x32_f16 v[98:101], v[18:21], v[192:195], v[98:101]
	v_mfma_f32_16x16x32_f16 v[102:105], v[22:25], v[192:195], v[102:105]
	v_mfma_f32_16x16x32_f16 v[106:109], v[26:29], v[192:195], v[106:109]
	v_mfma_f32_16x16x32_f16 v[110:113], v[30:33], v[192:195], v[110:113]
	s_waitcnt lgkmcnt(2)
	v_mfma_f32_16x16x32_f16 v[114:117], v[18:21], v[196:199], v[114:117]
	v_mfma_f32_16x16x32_f16 v[118:121], v[22:25], v[196:199], v[118:121]
	v_mfma_f32_16x16x32_f16 v[122:125], v[26:29], v[196:199], v[122:125]
	v_mfma_f32_16x16x32_f16 v[126:129], v[30:33], v[196:199], v[126:129]
	s_waitcnt lgkmcnt(1)
	v_mfma_f32_16x16x32_f16 v[130:133], v[18:21], v[200:203], v[130:133]
	v_mfma_f32_16x16x32_f16 v[134:137], v[22:25], v[200:203], v[134:137]
	v_mfma_f32_16x16x32_f16 v[138:141], v[26:29], v[200:203], v[138:141]
	s_waitcnt lgkmcnt(0)
	v_mfma_f32_16x16x32_f16 v[2:5], v[18:21], v[204:207], v[2:5]
	v_mfma_f32_16x16x32_f16 v[6:9], v[22:25], v[204:207], v[6:9]
	v_mfma_f32_16x16x32_f16 v[10:13], v[26:29], v[204:207], v[10:13]
	v_mfma_f32_16x16x32_f16 v[14:17], v[30:33], v[204:207], v[14:17]
	v_mfma_f32_16x16x32_f16 v[142:145], v[30:33], v[200:203], v[142:145]
	s_setprio 0
	s_or_b32 s7, s49, s48
	s_lshl_b32 s0, s7, 12
	v_lshl_add_u64 v[26:27], v[166:167], 0, s[0:1]
	global_load_dwordx4 v[18:21], v[26:27], off
	global_load_dwordx4 v[22:25], v[26:27], off offset:1024
	global_load_dwordx4 v[30:33], v[26:27], off offset:2048
	global_load_dwordx4 v[192:195], v[26:27], off offset:3072
	v_lshl_add_u32 v166, s2, 10, v191
	ds_read_b128 v[26:29], v166
	ds_read_b128 v[196:199], v166 offset:16384
	ds_read_b128 v[200:203], v166 offset:32768
	ds_read_b128 v[204:207], v166 offset:49152
	s_setprio 1
	s_waitcnt vmcnt(11) lgkmcnt(3)
	v_mfma_f32_16x16x32_f16 v[34:37], v[162:165], v[26:29], v[34:37]
	s_waitcnt vmcnt(10)
	v_mfma_f32_16x16x32_f16 v[38:41], v[168:171], v[26:29], v[38:41]
	s_waitcnt vmcnt(9)
	v_mfma_f32_16x16x32_f16 v[42:45], v[172:175], v[26:29], v[42:45]
	s_waitcnt vmcnt(8)
	v_mfma_f32_16x16x32_f16 v[26:29], v[176:179], v[26:29], v[46:49]
	s_waitcnt lgkmcnt(2)
	v_mfma_f32_16x16x32_f16 v[46:49], v[162:165], v[196:199], v[50:53]
	v_mfma_f32_16x16x32_f16 v[50:53], v[168:171], v[196:199], v[54:57]
	v_mfma_f32_16x16x32_f16 v[54:57], v[172:175], v[196:199], v[58:61]
	v_mfma_f32_16x16x32_f16 v[58:61], v[176:179], v[196:199], v[62:65]
	s_waitcnt lgkmcnt(1)
	v_mfma_f32_16x16x32_f16 v[62:65], v[162:165], v[200:203], v[66:69]
	v_mfma_f32_16x16x32_f16 v[66:69], v[168:171], v[200:203], v[70:73]
	v_mfma_f32_16x16x32_f16 v[70:73], v[172:175], v[200:203], v[74:77]
	v_mfma_f32_16x16x32_f16 v[74:77], v[176:179], v[200:203], v[78:81]
	s_waitcnt lgkmcnt(0)
	v_mfma_f32_16x16x32_f16 v[78:81], v[162:165], v[204:207], v[82:85]
	v_mfma_f32_16x16x32_f16 v[82:85], v[168:171], v[204:207], v[86:89]
	v_mfma_f32_16x16x32_f16 v[86:89], v[172:175], v[204:207], v[90:93]
	v_mfma_f32_16x16x32_f16 v[90:93], v[176:179], v[204:207], v[94:97]
	s_setprio 0
	s_nop 1
	v_add_u32_e32 v94, 0x10000, v166
	v_add_u32_e32 v167, 0x14000, v166
	ds_read_b128 v[94:97], v94
	ds_read_b128 v[196:199], v167
	v_add_u32_e32 v167, 0x18000, v166
	v_add_u32_e32 v166, 0x1c000, v166
	ds_read_b128 v[200:203], v167
	ds_read_b128 v[204:207], v166
	s_setprio 1
	s_waitcnt lgkmcnt(3)
	v_mfma_f32_16x16x32_f16 v[98:101], v[162:165], v[94:97], v[98:101]
	v_mfma_f32_16x16x32_f16 v[102:105], v[168:171], v[94:97], v[102:105]
	v_mfma_f32_16x16x32_f16 v[106:109], v[172:175], v[94:97], v[106:109]
	v_mfma_f32_16x16x32_f16 v[94:97], v[176:179], v[94:97], v[110:113]
	s_waitcnt lgkmcnt(2)
	v_mfma_f32_16x16x32_f16 v[110:113], v[162:165], v[196:199], v[114:117]
	v_mfma_f32_16x16x32_f16 v[114:117], v[168:171], v[196:199], v[118:121]
	v_mfma_f32_16x16x32_f16 v[118:121], v[172:175], v[196:199], v[122:125]
	v_mfma_f32_16x16x32_f16 v[122:125], v[176:179], v[196:199], v[126:129]
	s_waitcnt lgkmcnt(1)
	v_mfma_f32_16x16x32_f16 v[126:129], v[162:165], v[200:203], v[130:133]
	v_mfma_f32_16x16x32_f16 v[130:133], v[168:171], v[200:203], v[134:137]
	v_mfma_f32_16x16x32_f16 v[134:137], v[172:175], v[200:203], v[138:141]
	v_mfma_f32_16x16x32_f16 v[138:141], v[176:179], v[200:203], v[142:145]
	s_waitcnt lgkmcnt(0)
	v_mfma_f32_16x16x32_f16 v[2:5], v[162:165], v[204:207], v[2:5]
	v_mfma_f32_16x16x32_f16 v[6:9], v[168:171], v[204:207], v[6:9]
	v_mfma_f32_16x16x32_f16 v[10:13], v[172:175], v[204:207], v[10:13]
	v_mfma_f32_16x16x32_f16 v[14:17], v[176:179], v[204:207], v[14:17]
	s_setprio 0
	v_lshl_add_u32 v174, s3, 10, v191
	ds_read_b128 v[142:145], v174
	ds_read_b128 v[162:165], v174 offset:16384
	ds_read_b128 v[166:169], v174 offset:32768
	ds_read_b128 v[170:173], v174 offset:49152
	s_setprio 1
	s_waitcnt vmcnt(7) lgkmcnt(3)
	v_mfma_f32_16x16x32_f16 v[34:37], v[146:149], v[142:145], v[34:37]
	s_waitcnt vmcnt(6)
	v_mfma_f32_16x16x32_f16 v[38:41], v[150:153], v[142:145], v[38:41]
	s_waitcnt vmcnt(5)
	v_mfma_f32_16x16x32_f16 v[42:45], v[154:157], v[142:145], v[42:45]
	s_waitcnt vmcnt(4)
	v_mfma_f32_16x16x32_f16 v[26:29], v[158:161], v[142:145], v[26:29]
	s_waitcnt lgkmcnt(2)
	v_mfma_f32_16x16x32_f16 v[46:49], v[146:149], v[162:165], v[46:49]
	v_mfma_f32_16x16x32_f16 v[50:53], v[150:153], v[162:165], v[50:53]
	v_mfma_f32_16x16x32_f16 v[54:57], v[154:157], v[162:165], v[54:57]
	v_mfma_f32_16x16x32_f16 v[58:61], v[158:161], v[162:165], v[58:61]
	s_waitcnt lgkmcnt(1)
	v_mfma_f32_16x16x32_f16 v[62:65], v[146:149], v[166:169], v[62:65]
	v_mfma_f32_16x16x32_f16 v[66:69], v[150:153], v[166:169], v[66:69]
	v_mfma_f32_16x16x32_f16 v[70:73], v[154:157], v[166:169], v[70:73]
	v_mfma_f32_16x16x32_f16 v[74:77], v[158:161], v[166:169], v[74:77]
	s_waitcnt lgkmcnt(0)
	v_mfma_f32_16x16x32_f16 v[78:81], v[146:149], v[170:173], v[78:81]
	v_mfma_f32_16x16x32_f16 v[82:85], v[150:153], v[170:173], v[82:85]
	v_mfma_f32_16x16x32_f16 v[86:89], v[154:157], v[170:173], v[86:89]
	v_mfma_f32_16x16x32_f16 v[162:165], v[158:161], v[170:173], v[90:93]
	s_setprio 0
	s_nop 1
	v_add_u32_e32 v90, 0x10000, v174
	v_add_u32_e32 v142, 0x14000, v174
	v_add_u32_e32 v166, 0x18000, v174
	v_add_u32_e32 v170, 0x1c000, v174
	ds_read_b128 v[90:93], v90
	ds_read_b128 v[142:145], v142
	ds_read_b128 v[166:169], v166
	ds_read_b128 v[170:173], v170
	s_setprio 1
	s_waitcnt lgkmcnt(0)
	v_mfma_f32_16x16x32_f16 v[2:5], v[146:149], v[170:173], v[2:5]
	v_mfma_f32_16x16x32_f16 v[6:9], v[150:153], v[170:173], v[6:9]
	v_mfma_f32_16x16x32_f16 v[10:13], v[154:157], v[170:173], v[10:13]
	v_mfma_f32_16x16x32_f16 v[14:17], v[158:161], v[170:173], v[14:17]
	v_mfma_f32_16x16x32_f16 v[174:177], v[146:149], v[90:93], v[98:101]
	v_mfma_f32_16x16x32_f16 v[196:199], v[150:153], v[90:93], v[102:105]
	v_mfma_f32_16x16x32_f16 v[200:203], v[154:157], v[90:93], v[106:109]
	v_mfma_f32_16x16x32_f16 v[204:207], v[158:161], v[90:93], v[94:97]
	v_mfma_f32_16x16x32_f16 v[208:211], v[146:149], v[142:145], v[110:113]
	v_mfma_f32_16x16x32_f16 v[212:215], v[150:153], v[142:145], v[114:117]
	v_mfma_f32_16x16x32_f16 v[216:219], v[154:157], v[142:145], v[118:121]
	v_mfma_f32_16x16x32_f16 v[220:223], v[158:161], v[142:145], v[122:125]
	v_mfma_f32_16x16x32_f16 v[224:227], v[146:149], v[166:169], v[126:129]
	v_mfma_f32_16x16x32_f16 v[228:231], v[150:153], v[166:169], v[130:133]
	v_mfma_f32_16x16x32_f16 v[232:235], v[154:157], v[166:169], v[134:137]
	v_mfma_f32_16x16x32_f16 v[166:169], v[158:161], v[166:169], v[138:141]
	s_setprio 0
	v_lshl_add_u32 v158, s7, 10, v191
	ds_read_b128 v[90:93], v158
	ds_read_b128 v[94:97], v158 offset:16384
	ds_read_b128 v[98:101], v158 offset:32768
	ds_read_b128 v[146:149], v158 offset:49152
	s_setprio 1
	s_waitcnt vmcnt(3) lgkmcnt(3)
	v_mfma_f32_16x16x32_f16 v[150:153], v[18:21], v[90:93], v[34:37]
	s_waitcnt vmcnt(2)
	v_mfma_f32_16x16x32_f16 v[138:141], v[22:25], v[90:93], v[38:41]
	s_waitcnt vmcnt(1)
	v_mfma_f32_16x16x32_f16 v[154:157], v[30:33], v[90:93], v[42:45]
	s_waitcnt vmcnt(0)
	v_mfma_f32_16x16x32_f16 v[142:145], v[192:195], v[90:93], v[26:29]
	s_waitcnt lgkmcnt(2)
	v_mfma_f32_16x16x32_f16 v[134:137], v[18:21], v[94:97], v[46:49]
	v_mfma_f32_16x16x32_f16 v[122:125], v[22:25], v[94:97], v[50:53]
	v_mfma_f32_16x16x32_f16 v[130:133], v[30:33], v[94:97], v[54:57]
	v_mfma_f32_16x16x32_f16 v[126:129], v[192:195], v[94:97], v[58:61]
	s_waitcnt lgkmcnt(1)
	v_mfma_f32_16x16x32_f16 v[118:121], v[18:21], v[98:101], v[62:65]
	v_mfma_f32_16x16x32_f16 v[106:109], v[22:25], v[98:101], v[66:69]
	v_mfma_f32_16x16x32_f16 v[114:117], v[30:33], v[98:101], v[70:73]
	v_mfma_f32_16x16x32_f16 v[110:113], v[192:195], v[98:101], v[74:77]
	s_waitcnt lgkmcnt(0)
	v_mfma_f32_16x16x32_f16 v[102:105], v[18:21], v[146:149], v[78:81]
	v_mfma_f32_16x16x32_f16 v[90:93], v[22:25], v[146:149], v[82:85]
	v_mfma_f32_16x16x32_f16 v[98:101], v[30:33], v[146:149], v[86:89]
	v_mfma_f32_16x16x32_f16 v[94:97], v[192:195], v[146:149], v[162:165]
	s_setprio 0
	v_add_u32_e32 v26, 0x10000, v158
	v_add_u32_e32 v34, 0x14000, v158
	v_add_u32_e32 v38, 0x18000, v158
	ds_read_b128 v[26:29], v26
	ds_read_b128 v[34:37], v34
	v_add_u32_e32 v42, 0x1c000, v158
	ds_read_b128 v[38:41], v38
	ds_read_b128 v[146:149], v42
	s_setprio 1
	s_waitcnt lgkmcnt(3)
	v_mfma_f32_16x16x32_f16 v[86:89], v[18:21], v[26:29], v[174:177]
	v_mfma_f32_16x16x32_f16 v[74:77], v[22:25], v[26:29], v[196:199]
	v_mfma_f32_16x16x32_f16 v[82:85], v[30:33], v[26:29], v[200:203]
	v_mfma_f32_16x16x32_f16 v[78:81], v[192:195], v[26:29], v[204:207]
	s_waitcnt lgkmcnt(2)
	v_mfma_f32_16x16x32_f16 v[70:73], v[18:21], v[34:37], v[208:211]
	v_mfma_f32_16x16x32_f16 v[58:61], v[22:25], v[34:37], v[212:215]
	v_mfma_f32_16x16x32_f16 v[66:69], v[30:33], v[34:37], v[216:219]
	v_mfma_f32_16x16x32_f16 v[62:65], v[192:195], v[34:37], v[220:223]
	s_waitcnt lgkmcnt(1)
	v_mfma_f32_16x16x32_f16 v[54:57], v[18:21], v[38:41], v[224:227]
	v_mfma_f32_16x16x32_f16 v[42:45], v[22:25], v[38:41], v[228:231]
	v_mfma_f32_16x16x32_f16 v[50:53], v[30:33], v[38:41], v[232:235]
	v_mfma_f32_16x16x32_f16 v[46:49], v[192:195], v[38:41], v[166:169]
	s_waitcnt lgkmcnt(0)
	v_mfma_f32_16x16x32_f16 v[26:29], v[18:21], v[146:149], v[2:5]
	v_mfma_f32_16x16x32_f16 v[2:5], v[22:25], v[146:149], v[6:9]
	v_mfma_f32_16x16x32_f16 v[22:25], v[30:33], v[146:149], v[10:13]
	v_mfma_f32_16x16x32_f16 v[6:9], v[192:195], v[146:149], v[14:17]
	s_setprio 0
	s_lshl_b64 s[0:1], s[42:43], 2
	s_add_u32 s0, s18, s0
	s_addc_u32 s1, s19, s1
	s_lshl_b32 s2, s42, 8
	s_ashr_i32 s3, s2, 31
	v_lshlrev_b32_e32 v146, 5, v187
	s_lshl_b64 s[2:3], s[2:3], 2
	v_and_or_b32 v10, v190, 12, v146
	s_add_u32 s12, s12, s2
	s_addc_u32 s13, s13, s3
	v_lshlrev_b32_e32 v10, 2, v10
	v_add_u32_e32 v254, 0x22640, v10
	ds_read_b128 v[34:37], v254
	ds_read_b128 v[14:17], v254 offset:64
	ds_read_b128 v[38:41], v254 offset:1024
	ds_read_b128 v[18:21], v254 offset:1088
	ds_read_b128 v[30:33], v254 offset:2048
	ds_read_b128 v[10:13], v254 offset:2112
	s_add_u32 s12, s14, s2
	s_addc_u32 s13, s15, s3
	s_add_u32 s2, s16, s2
	s_addc_u32 s3, s17, s3
	s_nop 0
	v_cmp_gt_u32_e32 vcc, 16, v189
	s_mov_b32 s2, s69
	v_mov_b32_e32 v216, 0x3d38aa3b
	v_mov_b32_e32 v217, 0x3d38aa3b
	v_mov_b32_e32 v218, 0xbcb8aa3b
	v_mov_b32_e32 v219, 0xbcb8aa3b
	v_mov_b32_e32 v222, 1.0
	v_mov_b32_e32 v223, 1.0
	v_mov_b32_e32 v224, 0x4038aa3b
	v_mov_b32_e32 v225, 0x4038aa3b
	v_mov_b32_e32 v226, 0xbfb8aa3b
	v_mov_b32_e32 v227, 0xbfb8aa3b
	v_lshlrev_b32_e32 v232, 9, v187
	v_lshlrev_b32_e32 v233, 2, v188
	v_add3_u32 v232, s24, v232, v233
	s_waitcnt vmcnt(0) lgkmcnt(0)
	v_pk_mul_f32 v[34:35], v[34:35], v[224:225]
	v_pk_mul_f32 v[36:37], v[36:37], v[224:225]
	v_pk_mul_f32 v[14:15], v[14:15], v[224:225]
	v_pk_mul_f32 v[16:17], v[16:17], v[224:225]
	v_pk_mul_f32 v[38:39], v[38:39], v[226:227]
	v_pk_mul_f32 v[40:41], v[40:41], v[226:227]
	v_pk_mul_f32 v[18:19], v[18:19], v[226:227]
	v_pk_mul_f32 v[20:21], v[20:21], v[226:227]
	v_pk_fma_f32 v[150:151], v[150:151], v[216:217], v[34:35]
	v_pk_fma_f32 v[154:155], v[154:155], v[218:219], v[38:39]
	v_min_f32_e32 v150, 0x42700000, v150
	v_min_f32_e32 v151, 0x42700000, v151
	v_min_f32_e32 v154, 0x42700000, v154
	v_min_f32_e32 v155, 0x42700000, v155
	v_pk_fma_f32 v[152:153], v[152:153], v[216:217], v[36:37]
	v_pk_fma_f32 v[156:157], v[156:157], v[218:219], v[40:41]
	v_min_f32_e32 v152, 0x42700000, v152
	v_min_f32_e32 v153, 0x42700000, v153
	v_min_f32_e32 v156, 0x42700000, v156
	v_min_f32_e32 v157, 0x42700000, v157
	v_exp_f32_e32 v150, v150
	v_exp_f32_e32 v151, v151
	v_exp_f32_e32 v154, v154
	v_exp_f32_e32 v155, v155
	v_exp_f32_e32 v152, v152
	v_exp_f32_e32 v153, v153
	v_exp_f32_e32 v156, v156
	v_exp_f32_e32 v157, v157
	v_pk_fma_f32 v[228:229], v[150:151], v[30:31], v[30:31] neg_lo:[0,0,1] neg_hi:[0,0,1]
	v_pk_add_f32 v[154:155], v[154:155], v[222:223]
	v_pk_fma_f32 v[150:151], v[150:151], v[154:155], v[154:155]
	v_pk_fma_f32 v[230:231], v[152:153], v[32:33], v[32:33] neg_lo:[0,0,1] neg_hi:[0,0,1]
	v_pk_add_f32 v[156:157], v[156:157], v[222:223]
	v_pk_fma_f32 v[152:153], v[152:153], v[156:157], v[156:157]
	v_rcp_f32_e32 v150, v150
	v_rcp_f32_e32 v151, v151
	v_rcp_f32_e32 v152, v152
	v_rcp_f32_e32 v153, v153
	v_pk_mul_f32 v[200:201], v[228:229], v[150:151]
	v_pk_fma_f32 v[200:201], v[230:231], v[152:153], v[200:201]
	v_pk_fma_f32 v[138:139], v[138:139], v[216:217], v[14:15]
	v_pk_fma_f32 v[142:143], v[142:143], v[218:219], v[18:19]
	v_min_f32_e32 v138, 0x42700000, v138
	v_min_f32_e32 v139, 0x42700000, v139
	v_min_f32_e32 v142, 0x42700000, v142
	v_min_f32_e32 v143, 0x42700000, v143
	v_pk_fma_f32 v[140:141], v[140:141], v[216:217], v[16:17]
	v_pk_fma_f32 v[144:145], v[144:145], v[218:219], v[20:21]
	v_min_f32_e32 v140, 0x42700000, v140
	v_min_f32_e32 v141, 0x42700000, v141
	v_min_f32_e32 v144, 0x42700000, v144
	v_min_f32_e32 v145, 0x42700000, v145
	v_exp_f32_e32 v138, v138
	v_exp_f32_e32 v139, v139
	v_exp_f32_e32 v142, v142
	v_exp_f32_e32 v143, v143
	v_exp_f32_e32 v140, v140
	v_exp_f32_e32 v141, v141
	v_exp_f32_e32 v144, v144
	v_exp_f32_e32 v145, v145
	v_pk_fma_f32 v[228:229], v[138:139], v[10:11], v[10:11] neg_lo:[0,0,1] neg_hi:[0,0,1]
	v_pk_add_f32 v[142:143], v[142:143], v[222:223]
	v_pk_fma_f32 v[138:139], v[138:139], v[142:143], v[142:143]
	v_pk_fma_f32 v[230:231], v[140:141], v[12:13], v[12:13] neg_lo:[0,0,1] neg_hi:[0,0,1]
	v_pk_add_f32 v[144:145], v[144:145], v[222:223]
	v_pk_fma_f32 v[140:141], v[140:141], v[144:145], v[144:145]
	v_rcp_f32_e32 v138, v138
	v_rcp_f32_e32 v139, v139
	v_rcp_f32_e32 v140, v140
	v_rcp_f32_e32 v141, v141
	v_pk_fma_f32 v[200:201], v[228:229], v[138:139], v[200:201]
	v_pk_fma_f32 v[200:201], v[230:231], v[140:141], v[200:201]
	v_pk_fma_f32 v[134:135], v[134:135], v[216:217], v[34:35]
	v_pk_fma_f32 v[130:131], v[130:131], v[218:219], v[38:39]
	v_min_f32_e32 v134, 0x42700000, v134
	v_min_f32_e32 v135, 0x42700000, v135
	v_min_f32_e32 v130, 0x42700000, v130
	v_min_f32_e32 v131, 0x42700000, v131
	v_pk_fma_f32 v[136:137], v[136:137], v[216:217], v[36:37]
	v_pk_fma_f32 v[132:133], v[132:133], v[218:219], v[40:41]
	v_min_f32_e32 v136, 0x42700000, v136
	v_min_f32_e32 v137, 0x42700000, v137
	v_min_f32_e32 v132, 0x42700000, v132
	v_min_f32_e32 v133, 0x42700000, v133
	v_exp_f32_e32 v134, v134
	v_exp_f32_e32 v135, v135
	v_exp_f32_e32 v130, v130
	v_exp_f32_e32 v131, v131
	v_exp_f32_e32 v136, v136
	v_exp_f32_e32 v137, v137
	v_exp_f32_e32 v132, v132
	v_exp_f32_e32 v133, v133
	v_pk_fma_f32 v[228:229], v[134:135], v[30:31], v[30:31] neg_lo:[0,0,1] neg_hi:[0,0,1]
	v_pk_add_f32 v[130:131], v[130:131], v[222:223]
	v_pk_fma_f32 v[134:135], v[134:135], v[130:131], v[130:131]
	v_pk_fma_f32 v[230:231], v[136:137], v[32:33], v[32:33] neg_lo:[0,0,1] neg_hi:[0,0,1]
	v_pk_add_f32 v[132:133], v[132:133], v[222:223]
	v_pk_fma_f32 v[136:137], v[136:137], v[132:133], v[132:133]
	v_rcp_f32_e32 v134, v134
	v_rcp_f32_e32 v135, v135
	v_rcp_f32_e32 v136, v136
	v_rcp_f32_e32 v137, v137
	v_pk_mul_f32 v[202:203], v[228:229], v[134:135]
	v_pk_fma_f32 v[202:203], v[230:231], v[136:137], v[202:203]
	v_pk_fma_f32 v[122:123], v[122:123], v[216:217], v[14:15]
	v_pk_fma_f32 v[126:127], v[126:127], v[218:219], v[18:19]
	v_min_f32_e32 v122, 0x42700000, v122
	v_min_f32_e32 v123, 0x42700000, v123
	v_min_f32_e32 v126, 0x42700000, v126
	v_min_f32_e32 v127, 0x42700000, v127
	v_pk_fma_f32 v[124:125], v[124:125], v[216:217], v[16:17]
	v_pk_fma_f32 v[128:129], v[128:129], v[218:219], v[20:21]
	v_min_f32_e32 v124, 0x42700000, v124
	v_min_f32_e32 v125, 0x42700000, v125
	v_min_f32_e32 v128, 0x42700000, v128
	v_min_f32_e32 v129, 0x42700000, v129
	v_exp_f32_e32 v122, v122
	v_exp_f32_e32 v123, v123
	v_exp_f32_e32 v126, v126
	v_exp_f32_e32 v127, v127
	v_exp_f32_e32 v124, v124
	v_exp_f32_e32 v125, v125
	v_exp_f32_e32 v128, v128
	v_exp_f32_e32 v129, v129
	v_pk_fma_f32 v[228:229], v[122:123], v[10:11], v[10:11] neg_lo:[0,0,1] neg_hi:[0,0,1]
	v_pk_add_f32 v[126:127], v[126:127], v[222:223]
	v_pk_fma_f32 v[122:123], v[122:123], v[126:127], v[126:127]
	v_pk_fma_f32 v[230:231], v[124:125], v[12:13], v[12:13] neg_lo:[0,0,1] neg_hi:[0,0,1]
	v_pk_add_f32 v[128:129], v[128:129], v[222:223]
	v_pk_fma_f32 v[124:125], v[124:125], v[128:129], v[128:129]
	v_rcp_f32_e32 v122, v122
	v_rcp_f32_e32 v123, v123
	v_rcp_f32_e32 v124, v124
	v_rcp_f32_e32 v125, v125
	v_pk_fma_f32 v[202:203], v[228:229], v[122:123], v[202:203]
	v_pk_fma_f32 v[202:203], v[230:231], v[124:125], v[202:203]
	v_pk_fma_f32 v[118:119], v[118:119], v[216:217], v[34:35]
	v_pk_fma_f32 v[114:115], v[114:115], v[218:219], v[38:39]
	v_min_f32_e32 v118, 0x42700000, v118
	v_min_f32_e32 v119, 0x42700000, v119
	v_min_f32_e32 v114, 0x42700000, v114
	v_min_f32_e32 v115, 0x42700000, v115
	v_pk_fma_f32 v[120:121], v[120:121], v[216:217], v[36:37]
	v_pk_fma_f32 v[116:117], v[116:117], v[218:219], v[40:41]
	v_min_f32_e32 v120, 0x42700000, v120
	v_min_f32_e32 v121, 0x42700000, v121
	v_min_f32_e32 v116, 0x42700000, v116
	v_min_f32_e32 v117, 0x42700000, v117
	v_exp_f32_e32 v118, v118
	v_exp_f32_e32 v119, v119
	v_exp_f32_e32 v114, v114
	v_exp_f32_e32 v115, v115
	v_exp_f32_e32 v120, v120
	v_exp_f32_e32 v121, v121
	v_exp_f32_e32 v116, v116
	v_exp_f32_e32 v117, v117
	v_pk_fma_f32 v[228:229], v[118:119], v[30:31], v[30:31] neg_lo:[0,0,1] neg_hi:[0,0,1]
	v_pk_add_f32 v[114:115], v[114:115], v[222:223]
	v_pk_fma_f32 v[118:119], v[118:119], v[114:115], v[114:115]
	v_pk_fma_f32 v[230:231], v[120:121], v[32:33], v[32:33] neg_lo:[0,0,1] neg_hi:[0,0,1]
	v_pk_add_f32 v[116:117], v[116:117], v[222:223]
	v_pk_fma_f32 v[120:121], v[120:121], v[116:117], v[116:117]
	v_rcp_f32_e32 v118, v118
	v_rcp_f32_e32 v119, v119
	v_rcp_f32_e32 v120, v120
	v_rcp_f32_e32 v121, v121
	v_pk_mul_f32 v[204:205], v[228:229], v[118:119]
	v_pk_fma_f32 v[204:205], v[230:231], v[120:121], v[204:205]
	v_pk_fma_f32 v[106:107], v[106:107], v[216:217], v[14:15]
	v_pk_fma_f32 v[110:111], v[110:111], v[218:219], v[18:19]
	v_min_f32_e32 v106, 0x42700000, v106
	v_min_f32_e32 v107, 0x42700000, v107
	v_min_f32_e32 v110, 0x42700000, v110
	v_min_f32_e32 v111, 0x42700000, v111
	v_pk_fma_f32 v[108:109], v[108:109], v[216:217], v[16:17]
	v_pk_fma_f32 v[112:113], v[112:113], v[218:219], v[20:21]
	v_min_f32_e32 v108, 0x42700000, v108
	v_min_f32_e32 v109, 0x42700000, v109
	v_min_f32_e32 v112, 0x42700000, v112
	v_min_f32_e32 v113, 0x42700000, v113
	v_exp_f32_e32 v106, v106
	v_exp_f32_e32 v107, v107
	v_exp_f32_e32 v110, v110
	v_exp_f32_e32 v111, v111
	v_exp_f32_e32 v108, v108
	v_exp_f32_e32 v109, v109
	v_exp_f32_e32 v112, v112
	v_exp_f32_e32 v113, v113
	v_pk_fma_f32 v[228:229], v[106:107], v[10:11], v[10:11] neg_lo:[0,0,1] neg_hi:[0,0,1]
	v_pk_add_f32 v[110:111], v[110:111], v[222:223]
	v_pk_fma_f32 v[106:107], v[106:107], v[110:111], v[110:111]
	v_pk_fma_f32 v[230:231], v[108:109], v[12:13], v[12:13] neg_lo:[0,0,1] neg_hi:[0,0,1]
	v_pk_add_f32 v[112:113], v[112:113], v[222:223]
	v_pk_fma_f32 v[108:109], v[108:109], v[112:113], v[112:113]
	v_rcp_f32_e32 v106, v106
	v_rcp_f32_e32 v107, v107
	v_rcp_f32_e32 v108, v108
	v_rcp_f32_e32 v109, v109
	v_pk_fma_f32 v[204:205], v[228:229], v[106:107], v[204:205]
	v_pk_fma_f32 v[204:205], v[230:231], v[108:109], v[204:205]
	v_pk_fma_f32 v[102:103], v[102:103], v[216:217], v[34:35]
	v_pk_fma_f32 v[98:99], v[98:99], v[218:219], v[38:39]
	v_min_f32_e32 v102, 0x42700000, v102
	v_min_f32_e32 v103, 0x42700000, v103
	v_min_f32_e32 v98, 0x42700000, v98
	v_min_f32_e32 v99, 0x42700000, v99
	v_pk_fma_f32 v[104:105], v[104:105], v[216:217], v[36:37]
	v_pk_fma_f32 v[100:101], v[100:101], v[218:219], v[40:41]
	v_min_f32_e32 v104, 0x42700000, v104
	v_min_f32_e32 v105, 0x42700000, v105
	v_min_f32_e32 v100, 0x42700000, v100
	v_min_f32_e32 v101, 0x42700000, v101
	v_exp_f32_e32 v102, v102
	v_exp_f32_e32 v103, v103
	v_exp_f32_e32 v98, v98
	v_exp_f32_e32 v99, v99
	v_exp_f32_e32 v104, v104
	v_exp_f32_e32 v105, v105
	v_exp_f32_e32 v100, v100
	v_exp_f32_e32 v101, v101
	v_pk_fma_f32 v[228:229], v[102:103], v[30:31], v[30:31] neg_lo:[0,0,1] neg_hi:[0,0,1]
	v_pk_add_f32 v[98:99], v[98:99], v[222:223]
	v_pk_fma_f32 v[102:103], v[102:103], v[98:99], v[98:99]
	v_pk_fma_f32 v[230:231], v[104:105], v[32:33], v[32:33] neg_lo:[0,0,1] neg_hi:[0,0,1]
	v_pk_add_f32 v[100:101], v[100:101], v[222:223]
	v_pk_fma_f32 v[104:105], v[104:105], v[100:101], v[100:101]
	v_rcp_f32_e32 v102, v102
	v_rcp_f32_e32 v103, v103
	v_rcp_f32_e32 v104, v104
	v_rcp_f32_e32 v105, v105
	v_pk_mul_f32 v[206:207], v[228:229], v[102:103]
	v_pk_fma_f32 v[206:207], v[230:231], v[104:105], v[206:207]
	v_pk_fma_f32 v[90:91], v[90:91], v[216:217], v[14:15]
	v_pk_fma_f32 v[94:95], v[94:95], v[218:219], v[18:19]
	v_min_f32_e32 v90, 0x42700000, v90
	v_min_f32_e32 v91, 0x42700000, v91
	v_min_f32_e32 v94, 0x42700000, v94
	v_min_f32_e32 v95, 0x42700000, v95
	v_pk_fma_f32 v[92:93], v[92:93], v[216:217], v[16:17]
	v_pk_fma_f32 v[96:97], v[96:97], v[218:219], v[20:21]
	v_min_f32_e32 v92, 0x42700000, v92
	v_min_f32_e32 v93, 0x42700000, v93
	v_min_f32_e32 v96, 0x42700000, v96
	v_min_f32_e32 v97, 0x42700000, v97
	v_exp_f32_e32 v90, v90
	v_exp_f32_e32 v91, v91
	v_exp_f32_e32 v94, v94
	v_exp_f32_e32 v95, v95
	v_exp_f32_e32 v92, v92
	v_exp_f32_e32 v93, v93
	v_exp_f32_e32 v96, v96
	v_exp_f32_e32 v97, v97
	v_pk_fma_f32 v[228:229], v[90:91], v[10:11], v[10:11] neg_lo:[0,0,1] neg_hi:[0,0,1]
	v_pk_add_f32 v[94:95], v[94:95], v[222:223]
	v_pk_fma_f32 v[90:91], v[90:91], v[94:95], v[94:95]
	v_pk_fma_f32 v[230:231], v[92:93], v[12:13], v[12:13] neg_lo:[0,0,1] neg_hi:[0,0,1]
	v_pk_add_f32 v[96:97], v[96:97], v[222:223]
	v_pk_fma_f32 v[92:93], v[92:93], v[96:97], v[96:97]
	v_rcp_f32_e32 v90, v90
	v_rcp_f32_e32 v91, v91
	v_rcp_f32_e32 v92, v92
	v_rcp_f32_e32 v93, v93
	v_pk_fma_f32 v[206:207], v[228:229], v[90:91], v[206:207]
	v_pk_fma_f32 v[206:207], v[230:231], v[92:93], v[206:207]
	v_pk_fma_f32 v[86:87], v[86:87], v[216:217], v[34:35]
	v_pk_fma_f32 v[82:83], v[82:83], v[218:219], v[38:39]
	v_min_f32_e32 v86, 0x42700000, v86
	v_min_f32_e32 v87, 0x42700000, v87
	v_min_f32_e32 v82, 0x42700000, v82
	v_min_f32_e32 v83, 0x42700000, v83
	v_pk_fma_f32 v[88:89], v[88:89], v[216:217], v[36:37]
	v_pk_fma_f32 v[84:85], v[84:85], v[218:219], v[40:41]
	v_min_f32_e32 v88, 0x42700000, v88
	v_min_f32_e32 v89, 0x42700000, v89
	v_min_f32_e32 v84, 0x42700000, v84
	v_min_f32_e32 v85, 0x42700000, v85
	v_exp_f32_e32 v86, v86
	v_exp_f32_e32 v87, v87
	v_exp_f32_e32 v82, v82
	v_exp_f32_e32 v83, v83
	v_exp_f32_e32 v88, v88
	v_exp_f32_e32 v89, v89
	v_exp_f32_e32 v84, v84
	v_exp_f32_e32 v85, v85
	v_pk_fma_f32 v[228:229], v[86:87], v[30:31], v[30:31] neg_lo:[0,0,1] neg_hi:[0,0,1]
	v_pk_add_f32 v[82:83], v[82:83], v[222:223]
	v_pk_fma_f32 v[86:87], v[86:87], v[82:83], v[82:83]
	v_pk_fma_f32 v[230:231], v[88:89], v[32:33], v[32:33] neg_lo:[0,0,1] neg_hi:[0,0,1]
	v_pk_add_f32 v[84:85], v[84:85], v[222:223]
	v_pk_fma_f32 v[88:89], v[88:89], v[84:85], v[84:85]
	v_rcp_f32_e32 v86, v86
	v_rcp_f32_e32 v87, v87
	v_rcp_f32_e32 v88, v88
	v_rcp_f32_e32 v89, v89
	v_pk_mul_f32 v[208:209], v[228:229], v[86:87]
	v_pk_fma_f32 v[208:209], v[230:231], v[88:89], v[208:209]
	v_pk_fma_f32 v[74:75], v[74:75], v[216:217], v[14:15]
	v_pk_fma_f32 v[78:79], v[78:79], v[218:219], v[18:19]
	v_min_f32_e32 v74, 0x42700000, v74
	v_min_f32_e32 v75, 0x42700000, v75
	v_min_f32_e32 v78, 0x42700000, v78
	v_min_f32_e32 v79, 0x42700000, v79
	v_pk_fma_f32 v[76:77], v[76:77], v[216:217], v[16:17]
	v_pk_fma_f32 v[80:81], v[80:81], v[218:219], v[20:21]
	v_min_f32_e32 v76, 0x42700000, v76
	v_min_f32_e32 v77, 0x42700000, v77
	v_min_f32_e32 v80, 0x42700000, v80
	v_min_f32_e32 v81, 0x42700000, v81
	v_exp_f32_e32 v74, v74
	v_exp_f32_e32 v75, v75
	v_exp_f32_e32 v78, v78
	v_exp_f32_e32 v79, v79
	v_exp_f32_e32 v76, v76
	v_exp_f32_e32 v77, v77
	v_exp_f32_e32 v80, v80
	v_exp_f32_e32 v81, v81
	v_pk_fma_f32 v[228:229], v[74:75], v[10:11], v[10:11] neg_lo:[0,0,1] neg_hi:[0,0,1]
	v_pk_add_f32 v[78:79], v[78:79], v[222:223]
	v_pk_fma_f32 v[74:75], v[74:75], v[78:79], v[78:79]
	v_pk_fma_f32 v[230:231], v[76:77], v[12:13], v[12:13] neg_lo:[0,0,1] neg_hi:[0,0,1]
	v_pk_add_f32 v[80:81], v[80:81], v[222:223]
	v_pk_fma_f32 v[76:77], v[76:77], v[80:81], v[80:81]
	v_rcp_f32_e32 v74, v74
	v_rcp_f32_e32 v75, v75
	v_rcp_f32_e32 v76, v76
	v_rcp_f32_e32 v77, v77
	v_pk_fma_f32 v[208:209], v[228:229], v[74:75], v[208:209]
	v_pk_fma_f32 v[208:209], v[230:231], v[76:77], v[208:209]
	v_pk_fma_f32 v[70:71], v[70:71], v[216:217], v[34:35]
	v_pk_fma_f32 v[66:67], v[66:67], v[218:219], v[38:39]
	v_min_f32_e32 v70, 0x42700000, v70
	v_min_f32_e32 v71, 0x42700000, v71
	v_min_f32_e32 v66, 0x42700000, v66
	v_min_f32_e32 v67, 0x42700000, v67
	v_pk_fma_f32 v[72:73], v[72:73], v[216:217], v[36:37]
	v_pk_fma_f32 v[68:69], v[68:69], v[218:219], v[40:41]
	v_min_f32_e32 v72, 0x42700000, v72
	v_min_f32_e32 v73, 0x42700000, v73
	v_min_f32_e32 v68, 0x42700000, v68
	v_min_f32_e32 v69, 0x42700000, v69
	v_exp_f32_e32 v70, v70
	v_exp_f32_e32 v71, v71
	v_exp_f32_e32 v66, v66
	v_exp_f32_e32 v67, v67
	v_exp_f32_e32 v72, v72
	v_exp_f32_e32 v73, v73
	v_exp_f32_e32 v68, v68
	v_exp_f32_e32 v69, v69
	v_pk_fma_f32 v[228:229], v[70:71], v[30:31], v[30:31] neg_lo:[0,0,1] neg_hi:[0,0,1]
	v_pk_add_f32 v[66:67], v[66:67], v[222:223]
	v_pk_fma_f32 v[70:71], v[70:71], v[66:67], v[66:67]
	v_pk_fma_f32 v[230:231], v[72:73], v[32:33], v[32:33] neg_lo:[0,0,1] neg_hi:[0,0,1]
	v_pk_add_f32 v[68:69], v[68:69], v[222:223]
	v_pk_fma_f32 v[72:73], v[72:73], v[68:69], v[68:69]
	v_rcp_f32_e32 v70, v70
	v_rcp_f32_e32 v71, v71
	v_rcp_f32_e32 v72, v72
	v_rcp_f32_e32 v73, v73
	v_pk_mul_f32 v[210:211], v[228:229], v[70:71]
	v_pk_fma_f32 v[210:211], v[230:231], v[72:73], v[210:211]
	v_pk_fma_f32 v[58:59], v[58:59], v[216:217], v[14:15]
	v_pk_fma_f32 v[62:63], v[62:63], v[218:219], v[18:19]
	v_min_f32_e32 v58, 0x42700000, v58
	v_min_f32_e32 v59, 0x42700000, v59
	v_min_f32_e32 v62, 0x42700000, v62
	v_min_f32_e32 v63, 0x42700000, v63
	v_pk_fma_f32 v[60:61], v[60:61], v[216:217], v[16:17]
	v_pk_fma_f32 v[64:65], v[64:65], v[218:219], v[20:21]
	v_min_f32_e32 v60, 0x42700000, v60
	v_min_f32_e32 v61, 0x42700000, v61
	v_min_f32_e32 v64, 0x42700000, v64
	v_min_f32_e32 v65, 0x42700000, v65
	v_exp_f32_e32 v58, v58
	v_exp_f32_e32 v59, v59
	v_exp_f32_e32 v62, v62
	v_exp_f32_e32 v63, v63
	v_exp_f32_e32 v60, v60
	v_exp_f32_e32 v61, v61
	v_exp_f32_e32 v64, v64
	v_exp_f32_e32 v65, v65
	v_pk_fma_f32 v[228:229], v[58:59], v[10:11], v[10:11] neg_lo:[0,0,1] neg_hi:[0,0,1]
	v_pk_add_f32 v[62:63], v[62:63], v[222:223]
	v_pk_fma_f32 v[58:59], v[58:59], v[62:63], v[62:63]
	v_pk_fma_f32 v[230:231], v[60:61], v[12:13], v[12:13] neg_lo:[0,0,1] neg_hi:[0,0,1]
	v_pk_add_f32 v[64:65], v[64:65], v[222:223]
	v_pk_fma_f32 v[60:61], v[60:61], v[64:65], v[64:65]
	v_rcp_f32_e32 v58, v58
	v_rcp_f32_e32 v59, v59
	v_rcp_f32_e32 v60, v60
	v_rcp_f32_e32 v61, v61
	v_pk_fma_f32 v[210:211], v[228:229], v[58:59], v[210:211]
	v_pk_fma_f32 v[210:211], v[230:231], v[60:61], v[210:211]
	v_pk_fma_f32 v[54:55], v[54:55], v[216:217], v[34:35]
	v_pk_fma_f32 v[50:51], v[50:51], v[218:219], v[38:39]
	v_min_f32_e32 v54, 0x42700000, v54
	v_min_f32_e32 v55, 0x42700000, v55
	v_min_f32_e32 v50, 0x42700000, v50
	v_min_f32_e32 v51, 0x42700000, v51
	v_pk_fma_f32 v[56:57], v[56:57], v[216:217], v[36:37]
	v_pk_fma_f32 v[52:53], v[52:53], v[218:219], v[40:41]
	v_min_f32_e32 v56, 0x42700000, v56
	v_min_f32_e32 v57, 0x42700000, v57
	v_min_f32_e32 v52, 0x42700000, v52
	v_min_f32_e32 v53, 0x42700000, v53
	v_exp_f32_e32 v54, v54
	v_exp_f32_e32 v55, v55
	v_exp_f32_e32 v50, v50
	v_exp_f32_e32 v51, v51
	v_exp_f32_e32 v56, v56
	v_exp_f32_e32 v57, v57
	v_exp_f32_e32 v52, v52
	v_exp_f32_e32 v53, v53
	v_pk_fma_f32 v[228:229], v[54:55], v[30:31], v[30:31] neg_lo:[0,0,1] neg_hi:[0,0,1]
	v_pk_add_f32 v[50:51], v[50:51], v[222:223]
	v_pk_fma_f32 v[54:55], v[54:55], v[50:51], v[50:51]
	v_pk_fma_f32 v[230:231], v[56:57], v[32:33], v[32:33] neg_lo:[0,0,1] neg_hi:[0,0,1]
	v_pk_add_f32 v[52:53], v[52:53], v[222:223]
	v_pk_fma_f32 v[56:57], v[56:57], v[52:53], v[52:53]
	v_rcp_f32_e32 v54, v54
	v_rcp_f32_e32 v55, v55
	v_rcp_f32_e32 v56, v56
	v_rcp_f32_e32 v57, v57
	v_pk_mul_f32 v[212:213], v[228:229], v[54:55]
	v_pk_fma_f32 v[212:213], v[230:231], v[56:57], v[212:213]
	v_pk_fma_f32 v[42:43], v[42:43], v[216:217], v[14:15]
	v_pk_fma_f32 v[46:47], v[46:47], v[218:219], v[18:19]
	v_min_f32_e32 v42, 0x42700000, v42
	v_min_f32_e32 v43, 0x42700000, v43
	v_min_f32_e32 v46, 0x42700000, v46
	v_min_f32_e32 v47, 0x42700000, v47
	v_pk_fma_f32 v[44:45], v[44:45], v[216:217], v[16:17]
	v_pk_fma_f32 v[48:49], v[48:49], v[218:219], v[20:21]
	v_min_f32_e32 v44, 0x42700000, v44
	v_min_f32_e32 v45, 0x42700000, v45
	v_min_f32_e32 v48, 0x42700000, v48
	v_min_f32_e32 v49, 0x42700000, v49
	v_exp_f32_e32 v42, v42
	v_exp_f32_e32 v43, v43
	v_exp_f32_e32 v46, v46
	v_exp_f32_e32 v47, v47
	v_exp_f32_e32 v44, v44
	v_exp_f32_e32 v45, v45
	v_exp_f32_e32 v48, v48
	v_exp_f32_e32 v49, v49
	v_pk_fma_f32 v[228:229], v[42:43], v[10:11], v[10:11] neg_lo:[0,0,1] neg_hi:[0,0,1]
	v_pk_add_f32 v[46:47], v[46:47], v[222:223]
	v_pk_fma_f32 v[42:43], v[42:43], v[46:47], v[46:47]
	v_pk_fma_f32 v[230:231], v[44:45], v[12:13], v[12:13] neg_lo:[0,0,1] neg_hi:[0,0,1]
	v_pk_add_f32 v[48:49], v[48:49], v[222:223]
	v_pk_fma_f32 v[44:45], v[44:45], v[48:49], v[48:49]
	v_rcp_f32_e32 v42, v42
	v_rcp_f32_e32 v43, v43
	v_rcp_f32_e32 v44, v44
	v_rcp_f32_e32 v45, v45
	v_pk_fma_f32 v[212:213], v[228:229], v[42:43], v[212:213]
	v_pk_fma_f32 v[212:213], v[230:231], v[44:45], v[212:213]
	v_pk_fma_f32 v[26:27], v[26:27], v[216:217], v[34:35]
	v_pk_fma_f32 v[22:23], v[22:23], v[218:219], v[38:39]
	v_min_f32_e32 v26, 0x42700000, v26
	v_min_f32_e32 v27, 0x42700000, v27
	v_min_f32_e32 v22, 0x42700000, v22
	v_min_f32_e32 v23, 0x42700000, v23
	v_pk_fma_f32 v[28:29], v[28:29], v[216:217], v[36:37]
	v_pk_fma_f32 v[24:25], v[24:25], v[218:219], v[40:41]
	v_min_f32_e32 v28, 0x42700000, v28
	v_min_f32_e32 v29, 0x42700000, v29
	v_min_f32_e32 v24, 0x42700000, v24
	v_min_f32_e32 v25, 0x42700000, v25
	v_exp_f32_e32 v26, v26
	v_exp_f32_e32 v27, v27
	v_exp_f32_e32 v22, v22
	v_exp_f32_e32 v23, v23
	v_exp_f32_e32 v28, v28
	v_exp_f32_e32 v29, v29
	v_exp_f32_e32 v24, v24
	v_exp_f32_e32 v25, v25
	v_pk_fma_f32 v[228:229], v[26:27], v[30:31], v[30:31] neg_lo:[0,0,1] neg_hi:[0,0,1]
	v_pk_add_f32 v[22:23], v[22:23], v[222:223]
	v_pk_fma_f32 v[26:27], v[26:27], v[22:23], v[22:23]
	v_pk_fma_f32 v[230:231], v[28:29], v[32:33], v[32:33] neg_lo:[0,0,1] neg_hi:[0,0,1]
	v_pk_add_f32 v[24:25], v[24:25], v[222:223]
	v_pk_fma_f32 v[28:29], v[28:29], v[24:25], v[24:25]
	v_rcp_f32_e32 v26, v26
	v_rcp_f32_e32 v27, v27
	v_rcp_f32_e32 v28, v28
	v_rcp_f32_e32 v29, v29
	v_pk_mul_f32 v[214:215], v[228:229], v[26:27]
	v_pk_fma_f32 v[214:215], v[230:231], v[28:29], v[214:215]
	v_pk_fma_f32 v[2:3], v[2:3], v[216:217], v[14:15]
	v_pk_fma_f32 v[6:7], v[6:7], v[218:219], v[18:19]
	v_min_f32_e32 v2, 0x42700000, v2
	v_min_f32_e32 v3, 0x42700000, v3
	v_min_f32_e32 v6, 0x42700000, v6
	v_min_f32_e32 v7, 0x42700000, v7
	v_pk_fma_f32 v[4:5], v[4:5], v[216:217], v[16:17]
	v_pk_fma_f32 v[8:9], v[8:9], v[218:219], v[20:21]
	v_min_f32_e32 v4, 0x42700000, v4
	v_min_f32_e32 v5, 0x42700000, v5
	v_min_f32_e32 v8, 0x42700000, v8
	v_min_f32_e32 v9, 0x42700000, v9
	v_exp_f32_e32 v2, v2
	v_exp_f32_e32 v3, v3
	v_exp_f32_e32 v6, v6
	v_exp_f32_e32 v7, v7
	v_exp_f32_e32 v4, v4
	v_exp_f32_e32 v5, v5
	v_exp_f32_e32 v8, v8
	v_exp_f32_e32 v9, v9
	v_pk_fma_f32 v[228:229], v[2:3], v[10:11], v[10:11] neg_lo:[0,0,1] neg_hi:[0,0,1]
	v_pk_add_f32 v[6:7], v[6:7], v[222:223]
	v_pk_fma_f32 v[2:3], v[2:3], v[6:7], v[6:7]
	v_pk_fma_f32 v[230:231], v[4:5], v[12:13], v[12:13] neg_lo:[0,0,1] neg_hi:[0,0,1]
	v_pk_add_f32 v[8:9], v[8:9], v[222:223]
	v_pk_fma_f32 v[4:5], v[4:5], v[8:9], v[8:9]
	v_rcp_f32_e32 v2, v2
	v_rcp_f32_e32 v3, v3
	v_rcp_f32_e32 v4, v4
	v_rcp_f32_e32 v5, v5
	v_pk_fma_f32 v[214:215], v[228:229], v[2:3], v[214:215]
	v_pk_fma_f32 v[214:215], v[230:231], v[4:5], v[214:215]
	v_add_f32_e32 v240, v200, v201
	v_add_f32_e32 v241, v202, v203
	v_add_f32_e32 v242, v204, v205
	v_add_f32_e32 v243, v206, v207
	v_add_f32_e32 v244, v208, v209
	v_add_f32_e32 v245, v210, v211
	v_add_f32_e32 v246, v212, v213
	v_add_f32_e32 v247, v214, v215
	ds_bpermute_b32 v200, v181, v240
	ds_bpermute_b32 v201, v181, v241
	ds_bpermute_b32 v202, v181, v242
	ds_bpermute_b32 v203, v181, v243
	ds_bpermute_b32 v204, v181, v244
	ds_bpermute_b32 v205, v181, v245
	ds_bpermute_b32 v206, v181, v246
	ds_bpermute_b32 v207, v181, v247
	s_waitcnt lgkmcnt(0)
	v_add_f32_e32 v240, v240, v200
	v_add_f32_e32 v241, v241, v201
	v_add_f32_e32 v242, v242, v202
	v_add_f32_e32 v243, v243, v203
	v_add_f32_e32 v244, v244, v204
	v_add_f32_e32 v245, v245, v205
	v_add_f32_e32 v246, v246, v206
	v_add_f32_e32 v247, v247, v207
	ds_bpermute_b32 v200, v183, v240
	ds_bpermute_b32 v201, v183, v241
	ds_bpermute_b32 v202, v183, v242
	ds_bpermute_b32 v203, v183, v243
	ds_bpermute_b32 v204, v183, v244
	ds_bpermute_b32 v205, v183, v245
	ds_bpermute_b32 v206, v183, v246
	ds_bpermute_b32 v207, v183, v247
	s_waitcnt lgkmcnt(0)
	v_add_f32_e32 v240, v240, v200
	v_add_f32_e32 v241, v241, v201
	v_add_f32_e32 v242, v242, v202
	v_add_f32_e32 v243, v243, v203
	v_add_f32_e32 v244, v244, v204
	v_add_f32_e32 v245, v245, v205
	v_add_f32_e32 v246, v246, v206
	v_add_f32_e32 v247, v247, v207
	s_and_saveexec_b64 s[64:65], vcc
	ds_write2_b32 v232, v240, v241 offset0:0 offset1:16
	ds_write2_b32 v232, v242, v243 offset0:32 offset1:48
	ds_write2_b32 v232, v244, v245 offset0:64 offset1:80
	ds_write2_b32 v232, v246, v247 offset0:96 offset1:112
	s_mov_b64 exec, s[64:65]
	v_mov_b32_e32 v4, 0
	v_lshlrev_b32_e32 v10, 2, v189
	v_mov_b32_e32 v11, v4
	v_and_b32_e32 v70, 0x1c0, v0
	s_waitcnt lgkmcnt(0)
	v_lshl_add_u64 v[2:3], s[44:45], 0, v[10:11]
	s_lshl_b64 s[0:1], s[42:43], 17
	v_lshlrev_b32_e32 v6, 8, v70
	v_mov_b32_e32 v7, v4
	v_lshl_add_u64 v[2:3], v[2:3], 0, s[0:1]
	v_lshl_add_u64 v[2:3], v[2:3], 0, v[6:7]
	s_movk_i32 s0, 0x1000
	v_add_co_u32_e32 v6, vcc, s0, v2
	s_movk_i32 s0, 0x2000
	s_nop 0
	v_addc_co_u32_e32 v7, vcc, 0, v3, vcc
	v_add_co_u32_e32 v8, vcc, s0, v2
	s_movk_i32 s0, 0x3000
	s_nop 0
	v_addc_co_u32_e32 v9, vcc, 0, v3, vcc
	global_load_dword v78, v[2:3], off
	global_load_dword v77, v[2:3], off offset:256
	global_load_dword v76, v[2:3], off offset:512
	global_load_dword v75, v[2:3], off offset:768
	global_load_dword v74, v[2:3], off offset:1024
	global_load_dword v73, v[2:3], off offset:1280
	global_load_dword v72, v[2:3], off offset:1536
	global_load_dword v71, v[2:3], off offset:1792
	global_load_dword v69, v[2:3], off offset:2048
	global_load_dword v65, v[2:3], off offset:2304
	global_load_dword v63, v[2:3], off offset:2560
	global_load_dword v62, v[2:3], off offset:2816
	global_load_dword v61, v[2:3], off offset:3072
	global_load_dword v51, v[2:3], off offset:3328
	global_load_dword v52, v[2:3], off offset:3584
	global_load_dword v53, v[2:3], off offset:3840
	v_add_co_u32_e32 v2, vcc, s0, v2
	global_load_dword v55, v[6:7], off offset:256
	global_load_dword v56, v[6:7], off offset:512
	global_load_dword v57, v[6:7], off offset:768
	global_load_dword v54, v[6:7], off offset:1024
	global_load_dword v48, v[6:7], off offset:1280
	global_load_dword v49, v[6:7], off offset:1536
	global_load_dword v50, v[6:7], off offset:1792
	global_load_dword v47, v[6:7], off offset:2048
	global_load_dword v43, v[8:9], off
	global_load_dword v44, v[8:9], off offset:256
	global_load_dword v45, v[8:9], off offset:512
	global_load_dword v46, v[8:9], off offset:768
	global_load_dword v42, v[8:9], off offset:1024
	global_load_dword v39, v[8:9], off offset:1280
	global_load_dword v40, v[8:9], off offset:1536
	global_load_dword v41, v[8:9], off offset:1792
	global_load_dword v33, v[8:9], off offset:2048
	global_load_dword v34, v[8:9], off offset:2304
	global_load_dword v35, v[8:9], off offset:2560
	global_load_dword v36, v[8:9], off offset:2816
	global_load_dword v32, v[8:9], off offset:3072
	global_load_dword v24, v[8:9], off offset:3328
	global_load_dword v25, v[8:9], off offset:3584
	global_load_dword v26, v[8:9], off offset:3840
	v_addc_co_u32_e32 v3, vcc, 0, v3, vcc
	global_load_dword v66, v[6:7], off offset:2304
	global_load_dword v67, v[6:7], off offset:2560
	global_load_dword v68, v[6:7], off offset:2816
	global_load_dword v64, v[6:7], off offset:3072
	global_load_dword v58, v[6:7], off offset:3328
	global_load_dword v59, v[6:7], off offset:3584
	global_load_dword v60, v[6:7], off offset:3840
	global_load_dword v28, v[2:3], off
	global_load_dword v29, v[2:3], off offset:256
	global_load_dword v30, v[2:3], off offset:512
	global_load_dword v31, v[2:3], off offset:768
	global_load_dword v27, v[2:3], off offset:1024
	global_load_dword v21, v[2:3], off offset:1280
	global_load_dword v22, v[2:3], off offset:1536
	global_load_dword v23, v[2:3], off offset:1792
	global_load_dword v16, v[2:3], off offset:2048
	global_load_dword v79, v[8:9], off offset:-4096
	global_load_dword v18, v[2:3], off offset:2304
	global_load_dword v19, v[2:3], off offset:2560
	global_load_dword v20, v[2:3], off offset:2816
	global_load_dword v17, v[2:3], off offset:3072
	global_load_dword v15, v[2:3], off offset:3328
	global_load_dword v13, v[2:3], off offset:3584
	global_load_dword v11, v[2:3], off offset:3840
	v_lshl_add_u32 v2, v189, 2, 0
	v_add_u32_e32 v5, 0x20000, v2
	s_waitcnt vmcnt(63) expcnt(7) lgkmcnt(15)
	s_barrier
	ds_read2st64_b32 v[2:3], v5 offset1:1
	ds_read2st64_b32 v[6:7], v5 offset0:2 offset1:3
	ds_read2st64_b32 v[8:9], v5 offset0:4 offset1:5
	ds_read2st64_b32 v[80:81], v5 offset0:6 offset1:7
	s_mov_b32 s7, 0
	s_waitcnt lgkmcnt(3)
	v_add_f32_e32 v2, s2, v2
	v_add_f32_e32 v3, s2, v3
	s_waitcnt lgkmcnt(2)
	v_add_f32_e32 v2, v2, v6
	v_add_f32_e32 v3, v3, v7
	s_waitcnt lgkmcnt(1)
	v_add_f32_e32 v2, v2, v8
	v_add_f32_e32 v6, v3, v9
	s_waitcnt lgkmcnt(0)
	v_add_f32_e32 v12, v2, v80
	ds_read2st64_b32 v[2:3], v5 offset0:8 offset1:9
	v_add_f32_e32 v14, v6, v81
	ds_read2st64_b32 v[6:7], v5 offset0:10 offset1:11
	ds_read2st64_b32 v[8:9], v5 offset0:12 offset1:13
	ds_read2st64_b32 v[80:81], v5 offset0:14 offset1:15
	v_cmp_gt_u32_e64 s[0:1], 64, v0
	s_waitcnt lgkmcnt(3)
	v_add_f32_e32 v2, v12, v2
	v_add_f32_e32 v3, v14, v3
	s_waitcnt lgkmcnt(2)
	v_add_f32_e32 v2, v2, v6
	v_add_f32_e32 v3, v3, v7
	s_waitcnt lgkmcnt(1)
	v_add_f32_e32 v2, v2, v8
	v_add_f32_e32 v3, v3, v9
	s_waitcnt lgkmcnt(0)
	v_add_f32_e32 v2, v2, v80
	v_add_f32_e32 v3, v3, v81
	v_max_f32_e32 v5, v2, v3
	s_nop 1
	v_max_f32_dpp v5, v5, v5 quad_perm:[1,0,3,2] row_mask:0xf bank_mask:0xf
	s_nop 1
	v_max_f32_dpp v5, v5, v5 quad_perm:[2,3,0,1] row_mask:0xf bank_mask:0xf
	s_nop 1
	v_max_f32_dpp v5, v5, v5 row_half_mirror row_mask:0xf bank_mask:0xf
	s_nop 1
	v_max_f32_dpp v5, v5, v5 row_mirror row_mask:0xf bank_mask:0xf
	ds_bpermute_b32 v6, v181, v5
	s_waitcnt lgkmcnt(0)
	v_max_f32_e32 v5, v5, v6
	ds_bpermute_b32 v6, v183, v5
	s_waitcnt lgkmcnt(0)
	v_max_f32_e32 v14, v5, v6
	v_sub_f32_e32 v2, v2, v14
	v_sub_f32_e32 v3, v3, v14
	v_mul_f32_e32 v2, 0x3fb8aa3b, v2
	v_mul_f32_e32 v3, 0x3fb8aa3b, v3
	v_exp_f32_e32 v2, v2
	v_exp_f32_e32 v3, v3
	s_nop 0
	v_add_f32_e32 v5, v2, v3
	s_nop 1
	v_add_f32_dpp v5, v5, v5 quad_perm:[1,0,3,2] row_mask:0xf bank_mask:0xf
	s_nop 1
	v_add_f32_dpp v5, v5, v5 quad_perm:[2,3,0,1] row_mask:0xf bank_mask:0xf
	s_nop 1
	v_add_f32_dpp v5, v5, v5 row_half_mirror row_mask:0xf bank_mask:0xf
	s_nop 1
	v_add_f32_dpp v5, v5, v5 row_mirror row_mask:0xf bank_mask:0xf
	ds_bpermute_b32 v6, v181, v5
	s_waitcnt lgkmcnt(0)
	v_add_f32_e32 v37, v5, v6
	ds_bpermute_b32 v38, v183, v37
	s_and_saveexec_b64 s[2:3], s[0:1]
	s_cbranch_execz .LBB5_166
	s_add_i32 s12, 0, 0x21000
	v_lshl_add_u32 v5, v189, 2, s12
	v_lshl_add_u32 v6, v0, 2, s12
	ds_write_b32 v5, v2
	ds_write_b32 v6, v3 offset:256
